# MLP2: residual + bias loads moved into first K-loop iteration under counted vmcnt; f16->f32 residual conversion moved to epilogue
# speedup vs baseline: 1.0099x; 1.0036x over previous
.LBB6_6:
	v_lshlrev_b32_e32 v1, 4, v0
	v_and_b32_e32 v2, 32, v0
	v_bitop3_b32 v1, v1, v2, 48 bitop3:0x6c
	v_lshrrev_b32_e32 v7, 3, v0
	v_bfe_u32 v3, v0, 2, 4
	v_lshrrev_b32_e32 v2, 1, v1
	v_and_b32_e32 v38, 48, v7
	v_lshrrev_b32_e32 v1, 1, v0
	v_or_b32_e32 v8, v38, v3
	v_and_b32_e32 v1, 32, v1
	v_mul_lo_u32 v9, s7, v8
	v_or_b32_e32 v6, v1, v2
	s_waitcnt lgkmcnt(0)
	v_mov_b32_e32 v4, s10
	v_mov_b32_e32 v5, s11
	v_add_lshl_u32 v48, v9, v6, 1
	v_mad_u64_u32 v[8:9], s[10:11], s26, v8, v[6:7]
	s_movk_i32 s10, 0x70
	s_nop 0
	v_bitop3_b32 v39, v7, s10, 64 bitop3:0xc8
	v_or_b32_e32 v7, v39, v3
	s_lshl_b32 s40, s20, 3
	v_mul_lo_u32 v9, s7, v7
	v_mul_lo_u32 v7, s26, v7
	s_abs_i32 s41, s40
	v_add_lshl_u32 v52, v9, v6, 1
	v_add_lshl_u32 v54, v7, v6, 1
	v_cvt_f32_u32_e32 v6, s41
	s_lshr_b32 s24, s33, 6
	s_lshl_b32 s42, s24, 10
	s_sub_i32 s24, 0, s41
	v_rcp_iflag_f32_e32 v6, v6
	s_add_i32 s21, s21, s5
	s_bfe_i32 s43, s20, 0x1001c
	s_abs_i32 s20, s21
	v_mul_f32_e32 v6, 0x4f7ffffe, v6
	v_cvt_u32_f32_e32 v6, v6
	s_lshl_b32 s10, s26, 7
	s_lshr_b32 s27, s33, 8
	s_ashr_i32 s23, s7, 31
	v_readfirstlane_b32 s44, v6
	s_mul_i32 s24, s24, s44
	s_mul_hi_u32 s24, s44, s24
	s_add_i32 s44, s44, s24
	s_mul_hi_u32 s24, s20, s44
	s_mul_i32 s25, s24, s41
	s_mov_b32 s22, s7
	s_ashr_i32 s5, s21, 31
	s_sub_i32 s20, s20, s25
	s_bfe_u32 s4, s33, 0x20006
	v_add_lshl_u32 v56, v8, s10, 1
	s_lshl_b64 s[10:11], s[22:23], 8
	s_lshl_b32 s28, s27, 6
	s_xor_b32 s5, s5, s43
	s_add_i32 s25, s24, 1
	s_sub_i32 s29, s20, s41
	s_cmp_ge_u32 s20, s41
	s_cselect_b32 s24, s25, s24
	s_cselect_b32 s20, s29, s20
	s_add_i32 s25, s24, 1
	s_cmp_ge_u32 s20, s41
	s_cselect_b32 s20, s25, s24
	s_xor_b32 s20, s20, s5
	s_sub_i32 s20, s20, s5
	s_lshl_b32 s24, s20, 3
	s_sub_i32 s5, s3, s24
	s_min_i32 s25, s5, 8
	s_abs_i32 s29, s25
	v_cvt_f32_u32_e32 v6, s29
	s_sub_i32 s31, 0, s29
	s_mul_i32 s20, s20, s40
	s_sub_i32 s20, s21, s20
	v_rcp_iflag_f32_e32 v6, v6
	s_abs_i32 s30, s20
	s_xor_b32 s21, s20, s25
	s_ashr_i32 s21, s21, 31
	v_mul_f32_e32 v6, 0x4f7ffffe, v6
	v_cvt_u32_f32_e32 v6, v6
	s_mul_i32 s46, s26, 0x180
	s_mul_hi_i32 s45, s26, 0x180
	v_and_b32_e32 v41, 15, v0
	v_readfirstlane_b32 s47, v6
	s_mul_i32 s31, s31, s47
	s_mul_hi_u32 s31, s47, s31
	s_add_i32 s47, s47, s31
	s_mul_hi_u32 s31, s30, s47
	s_mul_i32 s47, s31, s29
	s_sub_i32 s30, s30, s47
	s_add_i32 s47, s31, 1
	s_sub_i32 s48, s30, s29
	s_cmp_ge_u32 s30, s29
	s_cselect_b32 s31, s47, s31
	s_cselect_b32 s30, s48, s30
	s_add_i32 s47, s31, 1
	s_cmp_ge_u32 s30, s29
	s_cselect_b32 s29, s47, s31
	s_xor_b32 s29, s29, s21
	s_sub_i32 s58, s29, s21
	s_mul_i32 s21, s58, s25
	s_sub_i32 s20, s20, s21
	s_add_i32 s57, s20, s24
	s_ashr_i32 s20, s57, 31
	s_mul_i32 s20, s10, s20
	s_mul_hi_u32 s21, s10, s57
	s_add_i32 s24, s21, s20
	s_lshr_b64 s[20:21], s[22:23], 24
	s_mul_i32 s20, s20, s57
	s_add_i32 s24, s24, s20
	s_mul_i32 s20, s10, s57
	s_add_u32 s22, s12, s20
	s_addc_u32 s23, s13, s24
	s_ashr_i32 s20, s58, 31
	s_mul_i32 s20, s46, s20
	s_mul_hi_u32 s21, s46, s58
	s_add_i32 s20, s21, s20
	s_mul_i32 s21, s45, s58
	s_add_i32 s47, s42, 0
	s_add_i32 s20, s20, s21
	s_mul_i32 s21, s46, s58
	s_add_i32 s48, s47, 0x2000
	s_add_u32 s24, s14, s21
	s_addc_u32 s25, s15, s20
	s_lshl_b32 s20, s57, 7
	s_add_i32 s20, s20, s28
	v_bfe_u32 v40, v0, 4, 2
	s_mul_i32 s5, s4, 48
	s_mov_b32 m0, s47
	v_or_b32_e32 v14, s20, v41
	s_mul_i32 s20, s58, 0xc0
	global_load_lds_dwordx4 v48, s[22:23]
	s_mov_b32 m0, s48
	s_add_i32 s49, s47, 0x4000
	s_add_i32 s20, s20, s5
	v_lshlrev_b32_e32 v42, 2, v40
	v_lshlrev_b32_e32 v50, 1, v8
	global_load_lds_dwordx4 v52, s[22:23]
	s_mov_b32 m0, s49
	s_add_i32 s50, s47, 0x6000
	v_or_b32_e32 v6, s20, v42
	global_load_lds_dwordx4 v50, s[24:25]
	s_mov_b32 m0, s50
	s_add_i32 s51, s47, 0x8000
	v_ashrrev_i32_e32 v7, 31, v6
	global_load_lds_dwordx4 v54, s[24:25]
	s_mov_b32 m0, s51
	v_lshl_add_u64 v[4:5], v[6:7], 1, v[4:5]
	v_mad_i64_i32 v[6:7], s[20:21], v14, s39, 0
	v_or_b32_e32 v8, 16, v14
	global_load_lds_dwordx4 v56, s[24:25]
	v_lshl_add_u64 v[190:191], v[6:7], 1, v[4:5]
	v_mad_i64_i32 v[8:9], s[20:21], v8, s39, 0
	v_lshl_add_u64 v[192:193], v[8:9], 1, v[4:5]
	v_or_b32_e32 v6, 32, v14
	v_mad_i64_i32 v[6:7], s[20:21], v6, s39, 0
	v_lshl_add_u64 v[194:195], v[6:7], 1, v[4:5]
	v_or_b32_e32 v10, 48, v14
	v_mad_i64_i32 v[10:11], s[20:21], v10, s39, 0
	v_lshl_add_u64 v[196:197], v[10:11], 1, v[4:5]
	s_load_dword s52, s[0:1], 0x48
	v_mov_b32_e32 v49, 0
	v_mov_b32_e32 v53, v49
	v_mov_b32_e32 v51, v49
	v_mov_b32_e32 v55, v49
	v_mov_b32_e32 v57, v49
	s_mov_b32 s53, 0
	v_lshl_add_u64 v[24:25], s[22:23], 0, v[48:49]
	v_lshl_add_u64 v[22:23], s[22:23], 0, v[52:53]
	v_lshl_add_u64 v[20:21], s[24:25], 0, v[50:51]
	v_lshl_add_u64 v[18:19], s[24:25], 0, v[54:55]
	s_cmp_lg_u32 s27, 1
	v_lshl_add_u64 v[16:17], s[24:25], 0, v[56:57]
	s_cbranch_scc1 .LBB6_8
	s_barrier
.LBB6_8:
	s_mov_b64 s[20:21], 0x80
	s_add_i32 s54, s47, 0xa000
	v_lshl_add_u64 v[24:25], v[24:25], 0, s[20:21]
	s_mov_b32 m0, s54
	s_add_i32 s55, s47, 0xc000
	s_waitcnt vmcnt(0)
	s_barrier
	global_load_lds_dwordx4 v[24:25], off
	v_lshl_add_u64 v[22:23], v[22:23], 0, s[20:21]
	s_mov_b32 m0, s55
	s_add_i32 s56, s47, 0xe000
	global_load_lds_dwordx4 v[22:23], off
	v_lshl_add_u64 v[20:21], v[20:21], 0, s[20:21]
	s_mov_b32 m0, s56
	v_lshl_add_u64 v[18:19], v[18:19], 0, s[20:21]
	global_load_lds_dwordx4 v[20:21], off
	s_add_i32 m0, s47, 0x10000
	v_lshl_add_u64 v[16:17], v[16:17], 0, s[20:21]
	global_load_lds_dwordx4 v[18:19], off
	s_add_i32 m0, s47, 0x12000
	v_or_b32_e32 v126, s28, v41
	global_load_lds_dwordx4 v[16:17], off
	s_waitcnt vmcnt(5)
	v_lshlrev_b32_e32 v4, 4, v40
	s_movk_i32 s0, 0x3c0
	v_lshlrev_b32_e32 v5, 6, v126
	v_lshlrev_b32_e32 v6, 2, v126
	v_and_or_b32 v5, v5, s0, v4
	s_lshl_b32 s1, s27, 13
	v_and_b32_e32 v6, 32, v6
	v_bitop3_b32 v127, v5, s1, v6 bitop3:0xde
	v_lshlrev_b32_e32 v5, 6, v0
	v_lshlrev_b32_e32 v0, 2, v0
	v_and_or_b32 v4, v5, s0, v4
	s_mulk_i32 s4, 0x1800
	v_and_b32_e32 v0, 32, v0
	v_bitop3_b32 v128, s4, v4, v0 bitop3:0xf6
	v_add_u32_e32 v0, v38, v3
	v_add_u32_e32 v3, v39, v3
	v_or_b32_e32 v12, 0x80, v0
	v_mad_u64_u32 v[4:5], s[0:1], s7, v0, v[2:3]
	v_mad_u64_u32 v[6:7], s[0:1], s26, v0, v[2:3]
	v_mad_u64_u32 v[8:9], s[0:1], s7, v3, v[2:3]
	v_mad_u64_u32 v[10:11], s[0:1], s26, v3, v[2:3]
	v_mad_u64_u32 v[2:3], s[0:1], s26, v12, v[2:3]
	s_ashr_i32 s0, s6, 31
	s_lshr_b32 s0, s0, 26
	s_add_i32 s0, s6, s0
	s_ashr_i32 s59, s0, 6
	v_add_lshl_u32 v0, v4, v1, 1
	v_add_lshl_u32 v4, v8, v1, 1
	v_add_lshl_u32 v6, v6, v1, 1
	v_add_lshl_u32 v8, v10, v1, 1
	v_add_lshl_u32 v2, v2, v1, 1
	s_cmp_gt_i32 s6, 63
	v_mov_b32_e32 v1, v49
	s_mov_b64 s[0:1], 0x100
	s_cselect_b64 s[6:7], -1, 0
	v_lshl_add_u64 v[106:107], v[0:1], 0, s[0:1]
	v_mov_b32_e32 v5, v49
	v_mov_b32_e32 v7, v49
	v_mov_b32_e32 v9, v49
	v_mov_b32_e32 v3, v49
	s_add_i32 s62, 0, 0x14000
	v_add_u32_e32 v0, 0x4000, v128
	v_or_b32_e32 v129, s5, v42
	s_add_i32 s60, s59, -3
	s_waitcnt lgkmcnt(0)
	s_ashr_i32 s61, s52, 31
	v_lshl_add_u64 v[108:109], v[4:5], 0, s[0:1]
	v_lshl_add_u64 v[110:111], v[6:7], 0, s[0:1]
	v_lshl_add_u64 v[112:113], v[8:9], 0, s[0:1]
	v_lshl_add_u64 v[114:115], v[2:3], 0, s[0:1]
	v_add_u32_e32 v130, s62, v0
	s_barrier
	s_branch .LBB6_10
.LBB6_9:
	v_cvt_f32_f16_sdwa v101, v218 dst_sel:DWORD dst_unused:UNUSED_PAD src0_sel:WORD_1
	v_cvt_f32_f16_e32 v100, v218
	v_cvt_f32_f16_sdwa v103, v220 dst_sel:DWORD dst_unused:UNUSED_PAD src0_sel:WORD_1
	v_cvt_f32_f16_e32 v102, v220
	v_cvt_f32_f16_sdwa v105, v221 dst_sel:DWORD dst_unused:UNUSED_PAD src0_sel:WORD_1
	v_cvt_f32_f16_e32 v104, v221
	v_cvt_f32_f16_sdwa v85, v210 dst_sel:DWORD dst_unused:UNUSED_PAD src0_sel:WORD_1
	v_cvt_f32_f16_e32 v84, v210
	v_cvt_f32_f16_sdwa v87, v213 dst_sel:DWORD dst_unused:UNUSED_PAD src0_sel:WORD_1
	v_cvt_f32_f16_sdwa v89, v212 dst_sel:DWORD dst_unused:UNUSED_PAD src0_sel:WORD_1
	v_cvt_f32_f16_e32 v88, v212
	v_cvt_f32_f16_e32 v86, v213
	v_cvt_f32_f16_sdwa v95, v217 dst_sel:DWORD dst_unused:UNUSED_PAD src0_sel:WORD_1
	v_cvt_f32_f16_sdwa v97, v216 dst_sel:DWORD dst_unused:UNUSED_PAD src0_sel:WORD_1
	v_cvt_f32_f16_e32 v96, v216
	v_cvt_f32_f16_e32 v94, v217
	v_cvt_f32_f16_sdwa v99, v219 dst_sel:DWORD dst_unused:UNUSED_PAD src0_sel:WORD_1
	v_cvt_f32_f16_e32 v98, v219
	v_cvt_f32_f16_sdwa v59, v199 dst_sel:DWORD dst_unused:UNUSED_PAD src0_sel:WORD_1
	v_cvt_f32_f16_sdwa v61, v198 dst_sel:DWORD dst_unused:UNUSED_PAD src0_sel:WORD_1
	v_cvt_f32_f16_e32 v60, v198
	v_cvt_f32_f16_e32 v58, v199
	v_cvt_f32_f16_sdwa v63, v201 dst_sel:DWORD dst_unused:UNUSED_PAD src0_sel:WORD_1
	v_cvt_f32_f16_sdwa v65, v200 dst_sel:DWORD dst_unused:UNUSED_PAD src0_sel:WORD_1
	v_cvt_f32_f16_e32 v64, v200
	v_cvt_f32_f16_e32 v62, v201
	v_cvt_f32_f16_sdwa v67, v203 dst_sel:DWORD dst_unused:UNUSED_PAD src0_sel:WORD_1
	v_cvt_f32_f16_sdwa v69, v202 dst_sel:DWORD dst_unused:UNUSED_PAD src0_sel:WORD_1
	v_cvt_f32_f16_e32 v68, v202
	v_cvt_f32_f16_e32 v66, v203
	v_cvt_f32_f16_sdwa v71, v205 dst_sel:DWORD dst_unused:UNUSED_PAD src0_sel:WORD_1
	v_cvt_f32_f16_sdwa v73, v204 dst_sel:DWORD dst_unused:UNUSED_PAD src0_sel:WORD_1
	v_cvt_f32_f16_e32 v72, v204
	v_cvt_f32_f16_e32 v70, v205
	v_cvt_f32_f16_sdwa v75, v207 dst_sel:DWORD dst_unused:UNUSED_PAD src0_sel:WORD_1
	v_cvt_f32_f16_sdwa v77, v206 dst_sel:DWORD dst_unused:UNUSED_PAD src0_sel:WORD_1
	v_cvt_f32_f16_e32 v76, v206
	v_cvt_f32_f16_e32 v74, v207
	v_cvt_f32_f16_sdwa v79, v209 dst_sel:DWORD dst_unused:UNUSED_PAD src0_sel:WORD_1
	v_cvt_f32_f16_sdwa v81, v208 dst_sel:DWORD dst_unused:UNUSED_PAD src0_sel:WORD_1
	v_cvt_f32_f16_e32 v80, v208
	v_cvt_f32_f16_e32 v78, v209
	v_cvt_f32_f16_sdwa v83, v211 dst_sel:DWORD dst_unused:UNUSED_PAD src0_sel:WORD_1
	v_cvt_f32_f16_e32 v82, v211
	v_cvt_f32_f16_sdwa v91, v215 dst_sel:DWORD dst_unused:UNUSED_PAD src0_sel:WORD_1
	v_cvt_f32_f16_sdwa v93, v214 dst_sel:DWORD dst_unused:UNUSED_PAD src0_sel:WORD_1
	v_cvt_f32_f16_e32 v92, v214
	v_cvt_f32_f16_e32 v90, v215
	s_mul_i32 s22, s58, 0xc0
	v_add_u32_e32 v116, s22, v129
	v_ashrrev_i32_e32 v117, 31, v116
	v_lshlrev_b64 v[124:125], 2, v[116:117]
	v_lshl_add_u64 v[132:133], s[18:19], 0, v[124:125]
	v_lshl_add_u32 v131, s57, 7, v126
	v_mad_i64_i32 v[136:137], s[22:23], v131, s39, 0
	v_or_b32_e32 v138, 16, v131
	v_or_b32_e32 v140, 32, v131
	v_or_b32_e32 v131, 48, v131
	v_mad_i64_i32 v[138:139], s[22:23], v138, s39, 0
	v_mad_i64_i32 v[140:141], s[22:23], v140, s39, 0
	v_mad_i64_i32 v[142:143], s[22:23], v131, s39, 0
	v_lshl_add_u64 v[136:137], v[136:137], 2, s[8:9]
	v_lshl_add_u64 v[138:139], v[138:139], 2, s[8:9]
	v_lshl_add_u64 v[140:141], v[140:141], 2, s[8:9]
	v_lshl_add_u64 v[142:143], v[142:143], 2, s[8:9]
	v_lshl_add_u64 v[136:137], v[136:137], 0, v[124:125]
	v_lshl_add_u64 v[138:139], v[138:139], 0, v[124:125]
	v_lshl_add_u64 v[140:141], v[140:141], 0, v[124:125]
	v_lshl_add_u64 v[124:125], v[142:143], 0, v[124:125]
	s_mov_b32 s57, s64
	s_mov_b32 s58, s63
	s_mov_b64 s[24:25], s[4:5]
	s_mov_b64 s[22:23], s[26:27]
	s_mov_b64 vcc, s[0:1]
	v_pk_add_f32 v[42:43], v[42:43], v[224:225]
	v_pk_add_f32 v[40:41], v[40:41], v[222:223]
	v_pk_add_f32 v[46:47], v[46:47], v[228:229]
	v_pk_add_f32 v[44:45], v[44:45], v[226:227]
	v_pk_add_f32 v[38:39], v[38:39], v[232:233]
	v_pk_add_f32 v[36:37], v[36:37], v[230:231]
	v_pk_add_f32 v[34:35], v[34:35], v[224:225]
	v_pk_add_f32 v[32:33], v[32:33], v[222:223]
	v_pk_add_f32 v[30:31], v[30:31], v[228:229]
	v_pk_add_f32 v[28:29], v[28:29], v[226:227]
	v_pk_add_f32 v[26:27], v[26:27], v[232:233]
	v_pk_add_f32 v[24:25], v[24:25], v[230:231]
	v_pk_add_f32 v[142:143], v[22:23], v[224:225]
	v_pk_add_f32 v[144:145], v[20:21], v[222:223]
	v_pk_add_f32 v[146:147], v[18:19], v[228:229]
	v_pk_add_f32 v[148:149], v[16:17], v[226:227]
	v_pk_add_f32 v[150:151], v[14:15], v[232:233]
	v_pk_add_f32 v[152:153], v[12:13], v[230:231]
	v_pk_add_f32 v[118:119], v[10:11], v[224:225]
	v_pk_add_f32 v[116:117], v[8:9], v[222:223]
	v_pk_add_f32 v[122:123], v[6:7], v[228:229]
	v_pk_add_f32 v[120:121], v[4:5], v[226:227]
	v_pk_add_f32 v[134:135], v[2:3], v[232:233]
	v_pk_add_f32 v[132:133], v[0:1], v[230:231]
	v_pk_add_f32 v[2:3], v[42:43], v[58:59]
	v_pk_add_f32 v[0:1], v[40:41], v[60:61]
	v_pk_add_f32 v[6:7], v[46:47], v[62:63]
	v_pk_add_f32 v[4:5], v[44:45], v[64:65]
	v_pk_add_f32 v[10:11], v[38:39], v[66:67]
	v_pk_add_f32 v[8:9], v[36:37], v[68:69]
	v_pk_add_f32 v[14:15], v[34:35], v[70:71]
	v_pk_add_f32 v[12:13], v[32:33], v[72:73]
	v_pk_add_f32 v[18:19], v[30:31], v[74:75]
	v_pk_add_f32 v[16:17], v[28:29], v[76:77]
	v_pk_add_f32 v[22:23], v[26:27], v[78:79]
	v_pk_add_f32 v[20:21], v[24:25], v[80:81]
	v_pk_add_f32 v[26:27], v[142:143], v[82:83]
	v_pk_add_f32 v[24:25], v[144:145], v[84:85]
	v_pk_add_f32 v[30:31], v[146:147], v[86:87]
	v_pk_add_f32 v[28:29], v[148:149], v[88:89]
	v_pk_add_f32 v[34:35], v[150:151], v[90:91]
	v_pk_add_f32 v[32:33], v[152:153], v[92:93]
	v_pk_add_f32 v[38:39], v[118:119], v[94:95]
	v_pk_add_f32 v[36:37], v[116:117], v[96:97]
	v_pk_add_f32 v[42:43], v[122:123], v[98:99]
	v_pk_add_f32 v[40:41], v[120:121], v[100:101]
	v_pk_add_f32 v[46:47], v[134:135], v[104:105]
	v_pk_add_f32 v[44:45], v[132:133], v[102:103]
	global_store_dwordx4 v[136:137], v[0:3], off sc1
	global_store_dwordx4 v[136:137], v[4:7], off offset:64 sc1
	global_store_dwordx4 v[136:137], v[8:11], off offset:128 sc1
	global_store_dwordx4 v[138:139], v[12:15], off sc1
	global_store_dwordx4 v[138:139], v[16:19], off offset:64 sc1
	global_store_dwordx4 v[138:139], v[20:23], off offset:128 sc1
	global_store_dwordx4 v[140:141], v[24:27], off sc1
	global_store_dwordx4 v[140:141], v[28:31], off offset:64 sc1
	global_store_dwordx4 v[140:141], v[32:35], off offset:128 sc1
	global_store_dwordx4 v[124:125], v[36:39], off sc1
	global_store_dwordx4 v[124:125], v[40:43], off offset:64 sc1
	global_store_dwordx4 v[124:125], v[44:47], off offset:128 sc1
	s_cbranch_vccnz .LBB6_23

.LBB6_22:
	s_add_u32 s30, s22, s28
	s_addc_u32 s31, s23, s29
	s_add_u32 s30, s30, 0x180
	s_addc_u32 s31, s31, 0
	s_add_u32 s66, s24, s28
	s_addc_u32 s67, s25, s29
	s_add_u32 s68, s66, 0x180
	s_addc_u32 s69, s67, 0
	s_cmp_eq_u32 s60, s65
	s_cselect_b32 s67, s27, s31
	s_cselect_b32 s66, s26, s30
	s_cselect_b32 s31, s5, s69
	s_cselect_b32 s30, s4, s68
	s_add_i32 s68, s62, s42
	v_add_u32_e32 v131, 0, v128
	v_add_u32_e32 v182, 0, v127
	v_lshl_add_u64 v[180:181], v[116:117], 0, s[28:29]
	s_mov_b32 m0, s68
	ds_read_b128 v[132:135], v131 offset:16384
	ds_read_b128 v[136:139], v131 offset:17408
	ds_read_b128 v[140:143], v131 offset:18432
	ds_read_b128 v[144:147], v131 offset:19456
	ds_read_b128 v[148:151], v182
	ds_read_b128 v[152:155], v182 offset:1024
	ds_read_b128 v[156:159], v182 offset:2048
	ds_read_b128 v[160:163], v182 offset:3072
	ds_read_b128 v[164:167], v182 offset:4096
	ds_read_b128 v[168:171], v182 offset:5120
	ds_read_b128 v[172:175], v182 offset:6144
	ds_read_b128 v[176:179], v182 offset:7168
	global_load_lds_dwordx4 v[180:181], off
	v_lshl_add_u64 v[180:181], v[118:119], 0, s[28:29]
	s_add_i32 m0, s68, 0x2000
	s_nop 0
	global_load_lds_dwordx4 v[180:181], off
	s_barrier
	s_waitcnt lgkmcnt(0)
	s_setprio 1
	s_waitcnt lgkmcnt(0)
	v_mfma_f32_16x16x32_f16 v[40:43], v[132:135], v[148:151], v[40:43]
	v_mfma_f32_16x16x32_f16 v[44:47], v[140:143], v[148:151], v[44:47]
	v_mfma_f32_16x16x32_f16 v[32:35], v[132:135], v[156:159], v[32:35]
	v_mfma_f32_16x16x32_f16 v[28:31], v[140:143], v[156:159], v[28:31]
	v_mfma_f32_16x16x32_f16 v[20:23], v[132:135], v[164:167], v[20:23]
	v_mfma_f32_16x16x32_f16 v[16:19], v[140:143], v[164:167], v[16:19]
	v_mfma_f32_16x16x32_f16 v[8:11], v[132:135], v[172:175], v[8:11]
	v_mfma_f32_16x16x32_f16 v[4:7], v[140:143], v[172:175], v[4:7]
	v_mfma_f32_16x16x32_f16 v[40:43], v[136:139], v[152:155], v[40:43]
	v_mfma_f32_16x16x32_f16 v[44:47], v[144:147], v[152:155], v[44:47]
	v_mfma_f32_16x16x32_f16 v[32:35], v[136:139], v[160:163], v[32:35]
	v_mfma_f32_16x16x32_f16 v[28:31], v[144:147], v[160:163], v[28:31]
	v_mfma_f32_16x16x32_f16 v[20:23], v[136:139], v[168:171], v[20:23]
	v_mfma_f32_16x16x32_f16 v[16:19], v[144:147], v[168:171], v[16:19]
	v_mfma_f32_16x16x32_f16 v[8:11], v[136:139], v[176:179], v[8:11]
	v_mfma_f32_16x16x32_f16 v[4:7], v[144:147], v[176:179], v[4:7]
	s_setprio 0
	s_barrier
	v_lshl_add_u64 v[140:141], v[120:121], 0, s[28:29]
	s_add_i32 m0, s47, 0x18000
	ds_read_b128 v[132:135], v131 offset:20480
	ds_read_b128 v[136:139], v131 offset:21504
	global_load_lds_dwordx4 v[140:141], off
	v_lshl_add_u64 v[140:141], v[122:123], 0, s[28:29]
	s_add_i32 m0, s47, 0x1a000
	s_nop 0
	global_load_lds_dwordx4 v[140:141], off
	v_lshl_add_u64 v[140:141], v[124:125], 0, s[28:29]
	s_add_i32 m0, s47, 0x1c000
	s_nop 0
	global_load_lds_dwordx4 v[140:141], off
	s_cmp_lg_u32 s65, 0
	s_cbranch_scc1 .Lm2_norm_0
	s_mul_i32 s70, s58, 0xc0
	v_add_u32_e32 v234, s70, v129
	v_ashrrev_i32_e32 v235, 31, v234
	v_lshlrev_b64 v[234:235], 2, v[234:235]
	v_lshl_add_u64 v[234:235], s[18:19], 0, v[234:235]
	global_load_dwordx4 v[222:225], v[234:235], off
	global_load_dwordx4 v[226:229], v[234:235], off offset:64
	global_load_dwordx4 v[230:233], v[234:235], off offset:128
	global_load_dwordx2 v[198:199], v[190:191], off
	global_load_dwordx2 v[200:201], v[190:191], off offset:32
	global_load_dwordx2 v[202:203], v[190:191], off offset:64
	global_load_dwordx2 v[204:205], v[192:193], off
	s_waitcnt vmcnt(12)
	s_branch .Lm2_join_0

.Lm2_join_0:
	s_barrier
	s_waitcnt lgkmcnt(0)
	s_setprio 1
	s_waitcnt lgkmcnt(0)
	v_mfma_f32_16x16x32_f16 v[36:39], v[132:135], v[148:151], v[36:39]
	v_mfma_f32_16x16x32_f16 v[24:27], v[132:135], v[156:159], v[24:27]
	v_mfma_f32_16x16x32_f16 v[12:15], v[132:135], v[164:167], v[12:15]
	v_mfma_f32_16x16x32_f16 v[0:3], v[132:135], v[172:175], v[0:3]
	v_mfma_f32_16x16x32_f16 v[36:39], v[136:139], v[152:155], v[36:39]
	v_mfma_f32_16x16x32_f16 v[24:27], v[136:139], v[160:163], v[24:27]
	v_mfma_f32_16x16x32_f16 v[12:15], v[136:139], v[168:171], v[12:15]
	v_mfma_f32_16x16x32_f16 v[0:3], v[136:139], v[176:179], v[0:3]
	s_setprio 0
	s_barrier
	s_mov_b32 m0, s47
	v_lshl_add_u64 v[180:181], s[66:67], 0, v[48:49]
	ds_read_b128 v[132:135], v131 offset:57344
	ds_read_b128 v[136:139], v131 offset:58368
	ds_read_b128 v[140:143], v131 offset:59392
	ds_read_b128 v[144:147], v131 offset:60416
	ds_read_b128 v[148:151], v182 offset:40960
	ds_read_b128 v[152:155], v182 offset:41984
	ds_read_b128 v[156:159], v182 offset:43008
	ds_read_b128 v[160:163], v182 offset:44032
	ds_read_b128 v[164:167], v182 offset:45056
	ds_read_b128 v[168:171], v182 offset:46080
	ds_read_b128 v[172:175], v182 offset:47104
	ds_read_b128 v[176:179], v182 offset:48128
	global_load_lds_dwordx4 v[180:181], off
	v_lshl_add_u64 v[182:183], s[66:67], 0, v[52:53]
	s_mov_b32 m0, s48
	s_nop 0
	global_load_lds_dwordx4 v[182:183], off
	s_barrier
	s_waitcnt lgkmcnt(0)
	s_setprio 1
	s_waitcnt lgkmcnt(0)
	v_mfma_f32_16x16x32_f16 v[40:43], v[132:135], v[148:151], v[40:43]
	v_mfma_f32_16x16x32_f16 v[44:47], v[140:143], v[148:151], v[44:47]
	v_mfma_f32_16x16x32_f16 v[32:35], v[132:135], v[156:159], v[32:35]
	v_mfma_f32_16x16x32_f16 v[28:31], v[140:143], v[156:159], v[28:31]
	v_mfma_f32_16x16x32_f16 v[20:23], v[132:135], v[164:167], v[20:23]
	v_mfma_f32_16x16x32_f16 v[16:19], v[140:143], v[164:167], v[16:19]
	v_mfma_f32_16x16x32_f16 v[8:11], v[132:135], v[172:175], v[8:11]
	v_mfma_f32_16x16x32_f16 v[4:7], v[140:143], v[172:175], v[4:7]
	v_mfma_f32_16x16x32_f16 v[40:43], v[136:139], v[152:155], v[40:43]
	v_mfma_f32_16x16x32_f16 v[44:47], v[144:147], v[152:155], v[44:47]
	v_mfma_f32_16x16x32_f16 v[32:35], v[136:139], v[160:163], v[32:35]
	v_mfma_f32_16x16x32_f16 v[28:31], v[144:147], v[160:163], v[28:31]
	v_mfma_f32_16x16x32_f16 v[20:23], v[136:139], v[168:171], v[20:23]
	v_mfma_f32_16x16x32_f16 v[16:19], v[144:147], v[168:171], v[16:19]
	v_mfma_f32_16x16x32_f16 v[8:11], v[136:139], v[176:179], v[8:11]
	v_mfma_f32_16x16x32_f16 v[4:7], v[144:147], v[176:179], v[4:7]
	s_setprio 0
	s_barrier
	s_mov_b32 m0, s49
	v_lshl_add_u64 v[184:185], s[30:31], 0, v[50:51]
	ds_read_b128 v[132:135], v131 offset:61440
	ds_read_b128 v[136:139], v131 offset:62464
	global_load_lds_dwordx4 v[184:185], off
	v_lshl_add_u64 v[186:187], s[30:31], 0, v[54:55]
	s_mov_b32 m0, s50
	v_lshl_add_u64 v[188:189], s[30:31], 0, v[56:57]
	global_load_lds_dwordx4 v[186:187], off
	s_mov_b32 m0, s51
	s_nop 0
	global_load_lds_dwordx4 v[188:189], off
	s_cmp_lg_u32 s65, 0
	s_cbranch_scc1 .Lm2_norm_1
	global_load_dwordx2 v[206:207], v[192:193], off offset:32
	global_load_dwordx2 v[208:209], v[192:193], off offset:64
	global_load_dwordx2 v[210:211], v[194:195], off
	global_load_dwordx2 v[212:213], v[194:195], off offset:32
	s_waitcnt vmcnt(16)
	s_branch .Lm2_join_1

.Lm2_join_1:
	s_barrier
	s_waitcnt lgkmcnt(0)
	s_setprio 1
	s_waitcnt lgkmcnt(0)
	v_mfma_f32_16x16x32_f16 v[36:39], v[132:135], v[148:151], v[36:39]
	v_mfma_f32_16x16x32_f16 v[24:27], v[132:135], v[156:159], v[24:27]
	v_mfma_f32_16x16x32_f16 v[12:15], v[132:135], v[164:167], v[12:15]
	v_mfma_f32_16x16x32_f16 v[0:3], v[132:135], v[172:175], v[0:3]
	v_mfma_f32_16x16x32_f16 v[36:39], v[136:139], v[152:155], v[36:39]
	v_mfma_f32_16x16x32_f16 v[24:27], v[136:139], v[160:163], v[24:27]
	v_mfma_f32_16x16x32_f16 v[12:15], v[136:139], v[168:171], v[12:15]
	v_mfma_f32_16x16x32_f16 v[0:3], v[136:139], v[176:179], v[0:3]
	s_setprio 0
	s_barrier
	s_mov_b32 m0, s54
	v_add_u32_e32 v131, s62, v127
	v_lshl_add_u64 v[180:181], v[180:181], 0, s[20:21]
	ds_read_b128 v[132:135], v130
	ds_read_b128 v[136:139], v130 offset:1024
	ds_read_b128 v[140:143], v130 offset:2048
	ds_read_b128 v[144:147], v130 offset:3072
	ds_read_b128 v[148:151], v131
	ds_read_b128 v[152:155], v131 offset:1024
	ds_read_b128 v[156:159], v131 offset:2048
	ds_read_b128 v[160:163], v131 offset:3072
	ds_read_b128 v[164:167], v131 offset:4096
	ds_read_b128 v[168:171], v131 offset:5120
	ds_read_b128 v[172:175], v131 offset:6144
	ds_read_b128 v[176:179], v131 offset:7168
	global_load_lds_dwordx4 v[180:181], off
	v_lshl_add_u64 v[180:181], v[182:183], 0, s[20:21]
	s_mov_b32 m0, s55
	s_nop 0
	global_load_lds_dwordx4 v[180:181], off
	s_barrier
	s_waitcnt lgkmcnt(0)
	s_setprio 1
	s_waitcnt lgkmcnt(0)
	v_mfma_f32_16x16x32_f16 v[40:43], v[132:135], v[148:151], v[40:43]
	v_mfma_f32_16x16x32_f16 v[44:47], v[140:143], v[148:151], v[44:47]
	v_mfma_f32_16x16x32_f16 v[32:35], v[132:135], v[156:159], v[32:35]
	v_mfma_f32_16x16x32_f16 v[28:31], v[140:143], v[156:159], v[28:31]
	v_mfma_f32_16x16x32_f16 v[20:23], v[132:135], v[164:167], v[20:23]
	v_mfma_f32_16x16x32_f16 v[16:19], v[140:143], v[164:167], v[16:19]
	v_mfma_f32_16x16x32_f16 v[8:11], v[132:135], v[172:175], v[8:11]
	v_mfma_f32_16x16x32_f16 v[4:7], v[140:143], v[172:175], v[4:7]
	v_mfma_f32_16x16x32_f16 v[40:43], v[136:139], v[152:155], v[40:43]
	v_mfma_f32_16x16x32_f16 v[44:47], v[144:147], v[152:155], v[44:47]
	v_mfma_f32_16x16x32_f16 v[32:35], v[136:139], v[160:163], v[32:35]
	v_mfma_f32_16x16x32_f16 v[28:31], v[144:147], v[160:163], v[28:31]
	v_mfma_f32_16x16x32_f16 v[20:23], v[136:139], v[168:171], v[20:23]
	v_mfma_f32_16x16x32_f16 v[16:19], v[144:147], v[168:171], v[16:19]
	v_mfma_f32_16x16x32_f16 v[8:11], v[136:139], v[176:179], v[8:11]
	v_mfma_f32_16x16x32_f16 v[4:7], v[144:147], v[176:179], v[4:7]
	s_setprio 0
	s_barrier
	s_mov_b32 m0, s56
	v_lshl_add_u64 v[140:141], v[184:185], 0, s[20:21]
	ds_read_b128 v[132:135], v130 offset:4096
	ds_read_b128 v[136:139], v130 offset:5120
	global_load_lds_dwordx4 v[140:141], off
	v_lshl_add_u64 v[140:141], v[186:187], 0, s[20:21]
	s_add_i32 m0, s56, 0x2000
	s_nop 0
	global_load_lds_dwordx4 v[140:141], off
	v_lshl_add_u64 v[140:141], v[188:189], 0, s[20:21]
	s_add_i32 m0, s56, 0x4000
	s_nop 0
	global_load_lds_dwordx4 v[140:141], off
	s_cmp_lg_u32 s65, 0
	s_cbranch_scc1 .Lm2_norm_2
	global_load_dwordx2 v[214:215], v[194:195], off offset:64
	global_load_dwordx2 v[216:217], v[196:197], off
	global_load_dwordx2 v[218:219], v[196:197], off offset:32
	global_load_dwordx2 v[220:221], v[196:197], off offset:64
	s_waitcnt vmcnt(13)
	s_branch .Lm2_join_2

.Lm2_join_2:
	s_barrier
	s_waitcnt lgkmcnt(0)
	s_setprio 1
	s_waitcnt lgkmcnt(0)
	v_mfma_f32_16x16x32_f16 v[36:39], v[132:135], v[148:151], v[36:39]
	v_mfma_f32_16x16x32_f16 v[24:27], v[132:135], v[156:159], v[24:27]
	v_mfma_f32_16x16x32_f16 v[12:15], v[132:135], v[164:167], v[12:15]
	v_mfma_f32_16x16x32_f16 v[0:3], v[132:135], v[172:175], v[0:3]
	v_mfma_f32_16x16x32_f16 v[36:39], v[136:139], v[152:155], v[36:39]
	v_mfma_f32_16x16x32_f16 v[24:27], v[136:139], v[160:163], v[24:27]
	v_mfma_f32_16x16x32_f16 v[12:15], v[136:139], v[168:171], v[12:15]
	v_mfma_f32_16x16x32_f16 v[0:3], v[136:139], v[176:179], v[0:3]
	s_setprio 0
	s_barrier
	s_add_i32 s65, s65, 3
	s_add_u32 s28, s28, 0x180
	s_addc_u32 s29, s29, 0
	s_cmp_ge_i32 s65, s59
	s_cbranch_scc0 .LBB6_22
	s_branch .LBB6_9

	.amdhsa_kernel _Z9k_gemm192IN4g1927EpiResHEEvNS0_4GemmET_
		.amdhsa_group_segment_fixed_size 0
		.amdhsa_private_segment_fixed_size 0
		.amdhsa_kernarg_size 328
		.amdhsa_user_sgpr_count 2
		.amdhsa_user_sgpr_dispatch_ptr 0
		.amdhsa_user_sgpr_queue_ptr 0
		.amdhsa_user_sgpr_kernarg_segment_ptr 1
		.amdhsa_user_sgpr_dispatch_id 0
		.amdhsa_user_sgpr_kernarg_preload_length 0
		.amdhsa_user_sgpr_kernarg_preload_offset 0
		.amdhsa_user_sgpr_private_segment_size 0
		.amdhsa_uses_dynamic_stack 0
		.amdhsa_enable_private_segment 0
		.amdhsa_system_sgpr_workgroup_id_x 1
		.amdhsa_system_sgpr_workgroup_id_y 0
		.amdhsa_system_sgpr_workgroup_id_z 0
		.amdhsa_system_sgpr_workgroup_info 0
		.amdhsa_system_vgpr_workitem_id 0
		.amdhsa_next_free_vgpr 236
		.amdhsa_next_free_sgpr 72
		.amdhsa_accum_offset 236
		.amdhsa_reserve_vcc 1
		.amdhsa_float_round_mode_32 0
		.amdhsa_float_round_mode_16_64 0
		.amdhsa_float_denorm_mode_32 3
		.amdhsa_float_denorm_mode_16_64 3
		.amdhsa_dx10_clamp 1
		.amdhsa_ieee_mode 1
		.amdhsa_fp16_overflow 0
		.amdhsa_tg_split 0
		.amdhsa_exception_fp_ieee_invalid_op 0
		.amdhsa_exception_fp_denorm_src 0
		.amdhsa_exception_fp_ieee_div_zero 0
		.amdhsa_exception_fp_ieee_overflow 0
		.amdhsa_exception_fp_ieee_underflow 0
		.amdhsa_exception_fp_ieee_inexact 0
		.amdhsa_exception_int_div_zero 0
	.end_amdhsa_kernel

amdhsa.kernels:
  - .agpr_count:     0
    .args:
      - .offset:         0
        .size:           224
        .value_kind:     by_value
      - .actual_access:  read_only
        .address_space:  global
        .offset:         224
        .size:           8
        .value_kind:     global_buffer
      - .actual_access:  read_only
        .address_space:  global
        .offset:         232
        .size:           8
        .value_kind:     global_buffer
      - .actual_access:  read_only
        .address_space:  global
        .offset:         240
        .size:           8
        .value_kind:     global_buffer
      - .actual_access:  write_only
        .address_space:  global
        .offset:         248
        .size:           8
        .value_kind:     global_buffer
      - .offset:         256
        .size:           4
        .value_kind:     hidden_block_count_x
      - .offset:         260
        .size:           4
        .value_kind:     hidden_block_count_y
      - .offset:         264
        .size:           4
        .value_kind:     hidden_block_count_z
      - .offset:         268
        .size:           2
        .value_kind:     hidden_group_size_x
      - .offset:         270
        .size:           2
        .value_kind:     hidden_group_size_y
      - .offset:         272
        .size:           2
        .value_kind:     hidden_group_size_z
      - .offset:         274
        .size:           2
        .value_kind:     hidden_remainder_x
      - .offset:         276
        .size:           2
        .value_kind:     hidden_remainder_y
      - .offset:         278
        .size:           2
        .value_kind:     hidden_remainder_z
      - .offset:         296
        .size:           8
        .value_kind:     hidden_global_offset_x
      - .offset:         304
        .size:           8
        .value_kind:     hidden_global_offset_y
      - .offset:         312
        .size:           8
        .value_kind:     hidden_global_offset_z
      - .offset:         320
        .size:           2
        .value_kind:     hidden_grid_dims
    .group_segment_fixed_size: 16640
    .kernarg_segment_align: 8
    .kernarg_segment_size: 512
    .language:       OpenCL C
    .language_version:
      - 2
      - 0
    .max_flat_workgroup_size: 256
    .name:           _Z10k_prep_ln18PrepArgsPKfS1_S1_Pt
    .private_segment_fixed_size: 0
    .sgpr_count:     28
    .sgpr_spill_count: 0
    .symbol:         _Z10k_prep_ln18PrepArgsPKfS1_S1_Pt.kd
    .uniform_work_group_size: 1
    .uses_dynamic_stack: false
    .vgpr_count:     75
    .vgpr_spill_count: 0
    .wavefront_size: 64
  - .agpr_count:     0
    .args:
      - .actual_access:  read_only
        .address_space:  global
        .offset:         0
        .size:           8
        .value_kind:     global_buffer
      - .actual_access:  read_only
        .address_space:  global
        .offset:         8
        .size:           8
        .value_kind:     global_buffer
      - .actual_access:  read_only
        .address_space:  global
        .offset:         16
        .size:           8
        .value_kind:     global_buffer
      - .actual_access:  write_only
        .address_space:  global
        .offset:         24
        .size:           8
        .value_kind:     global_buffer
    .group_segment_fixed_size: 0
    .kernarg_segment_align: 8
    .kernarg_segment_size: 32
    .language:       OpenCL C
    .language_version:
      - 2
      - 0
    .max_flat_workgroup_size: 256
    .name:           _Z5k_ln2PKfS0_S0_Pt
    .private_segment_fixed_size: 0
    .sgpr_count:     18
    .sgpr_spill_count: 0
    .symbol:         _Z5k_ln2PKfS0_S0_Pt.kd
    .uniform_work_group_size: 1
    .uses_dynamic_stack: false
    .vgpr_count:     54
    .vgpr_spill_count: 0
    .wavefront_size: 64
  - .agpr_count:     0
    .args:
      - .actual_access:  read_only
        .address_space:  global
        .offset:         0
        .size:           8
        .value_kind:     global_buffer
      - .actual_access:  read_only
        .address_space:  global
        .offset:         8
        .size:           8
        .value_kind:     global_buffer
      - .actual_access:  read_only
        .address_space:  global
        .offset:         16
        .size:           8
        .value_kind:     global_buffer
      - .actual_access:  read_only
        .address_space:  global
        .offset:         24
        .size:           8
        .value_kind:     global_buffer
      - .actual_access:  read_only
        .address_space:  global
        .offset:         32
        .size:           8
        .value_kind:     global_buffer
      - .actual_access:  write_only
        .address_space:  global
        .offset:         40
        .size:           8
        .value_kind:     global_buffer
      - .offset:         48
        .size:           224
        .value_kind:     by_value
    .group_segment_fixed_size: 0
    .kernarg_segment_align: 8
    .kernarg_segment_size: 272
    .language:       OpenCL C
    .language_version:
      - 2
      - 0
    .max_flat_workgroup_size: 256
    .name:           _Z6k_attnPKtS0_S0_S0_S0_Pt8PrepArgs
    .private_segment_fixed_size: 0
    .sgpr_count:     30
    .sgpr_spill_count: 0
    .symbol:         _Z6k_attnPKtS0_S0_S0_S0_Pt8PrepArgs.kd
    .uniform_work_group_size: 1
    .uses_dynamic_stack: false
    .vgpr_count:     244
    .vgpr_spill_count: 0
    .wavefront_size: 64
  - .agpr_count:     0
    .args:
      - .offset:         0
        .size:           40
        .value_kind:     by_value
      - .offset:         40
        .size:           32
        .value_kind:     by_value
      - .offset:         72
        .size:           4
        .value_kind:     hidden_block_count_x
      - .offset:         76
        .size:           4
        .value_kind:     hidden_block_count_y
      - .offset:         80
        .size:           4
        .value_kind:     hidden_block_count_z
      - .offset:         84
        .size:           2
        .value_kind:     hidden_group_size_x
      - .offset:         86
        .size:           2
        .value_kind:     hidden_group_size_y
      - .offset:         88
        .size:           2
        .value_kind:     hidden_group_size_z
      - .offset:         90
        .size:           2
        .value_kind:     hidden_remainder_x
      - .offset:         92
        .size:           2
        .value_kind:     hidden_remainder_y
      - .offset:         94
        .size:           2
        .value_kind:     hidden_remainder_z
      - .offset:         112
        .size:           8
        .value_kind:     hidden_global_offset_x
      - .offset:         120
        .size:           8
        .value_kind:     hidden_global_offset_y
      - .offset:         128
        .size:           8
        .value_kind:     hidden_global_offset_z
      - .offset:         136
        .size:           2
        .value_kind:     hidden_grid_dims
      - .offset:         192
        .size:           4
        .value_kind:     hidden_dynamic_lds_size
    .group_segment_fixed_size: 0
    .kernarg_segment_align: 8
    .kernarg_segment_size: 328
    .language:       OpenCL C
    .language_version:
      - 2
      - 0
    .max_flat_workgroup_size: 512
    .name:           _Z9k_gemm192IN4g1926EpiQKVEEvNS0_4GemmET_
    .private_segment_fixed_size: 0
    .sgpr_count:     74
    .sgpr_spill_count: 0
    .symbol:         _Z9k_gemm192IN4g1926EpiQKVEEvNS0_4GemmET_.kd
    .uniform_work_group_size: 1
    .uses_dynamic_stack: false
    .vgpr_count:     156
    .vgpr_spill_count: 0
    .wavefront_size: 64
  - .agpr_count:     0
    .args:
      - .offset:         0
        .size:           40
        .value_kind:     by_value
      - .offset:         40
        .size:           48
        .value_kind:     by_value
      - .offset:         88
        .size:           4
        .value_kind:     hidden_block_count_x
      - .offset:         92
        .size:           4
        .value_kind:     hidden_block_count_y
      - .offset:         96
        .size:           4
        .value_kind:     hidden_block_count_z
      - .offset:         100
        .size:           2
        .value_kind:     hidden_group_size_x
      - .offset:         102
        .size:           2
        .value_kind:     hidden_group_size_y
      - .offset:         104
        .size:           2
        .value_kind:     hidden_group_size_z
      - .offset:         106
        .size:           2
        .value_kind:     hidden_remainder_x
      - .offset:         108
        .size:           2
        .value_kind:     hidden_remainder_y
      - .offset:         110
        .size:           2
        .value_kind:     hidden_remainder_z
      - .offset:         128
        .size:           8
        .value_kind:     hidden_global_offset_x
      - .offset:         136
        .size:           8
        .value_kind:     hidden_global_offset_y
      - .offset:         144
        .size:           8
        .value_kind:     hidden_global_offset_z
      - .offset:         152
        .size:           2
        .value_kind:     hidden_grid_dims
      - .offset:         208
        .size:           4
        .value_kind:     hidden_dynamic_lds_size
    .group_segment_fixed_size: 0
    .kernarg_segment_align: 8
    .kernarg_segment_size: 344
    .language:       OpenCL C
    .language_version:
      - 2
      - 0
    .max_flat_workgroup_size: 512
    .name:           _Z9k_gemm192IN4g19210EpiResStatEEvNS0_4GemmET_
    .private_segment_fixed_size: 0
    .sgpr_count:     78
    .sgpr_spill_count: 0
    .symbol:         _Z9k_gemm192IN4g19210EpiResStatEEvNS0_4GemmET_.kd
    .uniform_work_group_size: 1
    .uses_dynamic_stack: false
    .vgpr_count:     216
    .vgpr_spill_count: 0
    .wavefront_size: 64
  - .agpr_count:     0
    .args:
      - .offset:         0
        .size:           40
        .value_kind:     by_value
      - .offset:         40
        .size:           48
        .value_kind:     by_value
      - .offset:         88
        .size:           4
        .value_kind:     hidden_block_count_x
      - .offset:         92
        .size:           4
        .value_kind:     hidden_block_count_y
      - .offset:         96
        .size:           4
        .value_kind:     hidden_block_count_z
      - .offset:         100
        .size:           2
        .value_kind:     hidden_group_size_x
      - .offset:         102
        .size:           2
        .value_kind:     hidden_group_size_y
      - .offset:         104
        .size:           2
        .value_kind:     hidden_group_size_z
      - .offset:         106
        .size:           2
        .value_kind:     hidden_remainder_x
      - .offset:         108
        .size:           2
        .value_kind:     hidden_remainder_y
      - .offset:         110
        .size:           2
        .value_kind:     hidden_remainder_z
      - .offset:         128
        .size:           8
        .value_kind:     hidden_global_offset_x
      - .offset:         136
        .size:           8
        .value_kind:     hidden_global_offset_y
      - .offset:         144
        .size:           8
        .value_kind:     hidden_global_offset_z
      - .offset:         152
        .size:           2
        .value_kind:     hidden_grid_dims
      - .offset:         208
        .size:           4
        .value_kind:     hidden_dynamic_lds_size
    .group_segment_fixed_size: 0
    .kernarg_segment_align: 8
    .kernarg_segment_size: 344
    .language:       OpenCL C
    .language_version:
      - 2
      - 0
    .max_flat_workgroup_size: 512
    .name:           _Z9k_gemm128IN4g1289EpiGeluLNEEvNS0_4GemmET_
    .private_segment_fixed_size: 0
    .sgpr_count:     84
    .sgpr_spill_count: 0
    .symbol:         _Z9k_gemm128IN4g1289EpiGeluLNEEvNS0_4GemmET_.kd
    .uniform_work_group_size: 1
    .uses_dynamic_stack: false
    .vgpr_count:     170
    .vgpr_spill_count: 0
    .wavefront_size: 64
  - .agpr_count:     0
    .args:
      - .offset:         0
        .size:           40
        .value_kind:     by_value
      - .offset:         40
        .size:           32
        .value_kind:     by_value
      - .offset:         72
        .size:           4
        .value_kind:     hidden_block_count_x
      - .offset:         76
        .size:           4
        .value_kind:     hidden_block_count_y
      - .offset:         80
        .size:           4
        .value_kind:     hidden_block_count_z
      - .offset:         84
        .size:           2
        .value_kind:     hidden_group_size_x
      - .offset:         86
        .size:           2
        .value_kind:     hidden_group_size_y
      - .offset:         88
        .size:           2
        .value_kind:     hidden_group_size_z
      - .offset:         90
        .size:           2
        .value_kind:     hidden_remainder_x
      - .offset:         92
        .size:           2
        .value_kind:     hidden_remainder_y
      - .offset:         94
        .size:           2
        .value_kind:     hidden_remainder_z
      - .offset:         112
        .size:           8
        .value_kind:     hidden_global_offset_x
      - .offset:         120
        .size:           8
        .value_kind:     hidden_global_offset_y
      - .offset:         128
        .size:           8
        .value_kind:     hidden_global_offset_z
      - .offset:         136
        .size:           2
        .value_kind:     hidden_grid_dims
      - .offset:         192
        .size:           4
        .value_kind:     hidden_dynamic_lds_size
    .group_segment_fixed_size: 0
    .kernarg_segment_align: 8
    .kernarg_segment_size: 328
    .language:       OpenCL C
    .language_version:
      - 2
      - 0
    .max_flat_workgroup_size: 512
    .name:           _Z9k_gemm192IN4g1927EpiResHEEvNS0_4GemmET_
    .private_segment_fixed_size: 0
    .sgpr_count:     76
    .sgpr_spill_count: 0
    .symbol:         _Z9k_gemm192IN4g1927EpiResHEEvNS0_4GemmET_.kd
    .uniform_work_group_size: 1
    .uses_dynamic_stack: false
    .vgpr_count:     236
    .vgpr_spill_count: 0
    .wavefront_size: 64
